# baseline (speedup 1.0000x reference)
.LBB3_32:
	s_ashr_i32 s12, s2, 3
	s_lshl_b32 s6, s12, 1
	s_ashr_i32 s7, s6, 31
	s_lshl_b64 s[6:7], s[6:7], 2
	s_waitcnt lgkmcnt(0)
	s_add_u32 s8, s14, s6
	s_addc_u32 s9, s15, s7
	s_load_dwordx2 s[4:5], s[0:1], 0x10
	s_load_dwordx2 s[6:7], s[8:9], 0x0
	v_cmp_gt_u32_e32 vcc, 64, v0
	v_lshlrev_b32_e32 v1, 2, v0
	s_and_saveexec_b64 s[8:9], vcc
	v_lshl_or_b32 v2, s12, 6, v0
	v_ashrrev_i32_e32 v3, 31, v2
	v_lshlrev_b64 v[2:3], 2, v[2:3]
	v_lshl_add_u64 v[4:5], s[16:17], 0, v[2:3]
	v_lshl_add_u64 v[2:3], s[18:19], 0, v[2:3]
	global_load_dword v40, v[4:5], off
	global_load_dword v41, v[2:3], off
	v_add_u32_e32 v42, 0x50, v1
	s_or_b64 exec, exec, s[8:9]
	s_ashr_i32 s8, s2, 9
	s_ashr_i32 s9, s8, 31
	s_waitcnt lgkmcnt(0)
	s_lshl_b32 s3, s6, 6
	s_lshl_b64 s[10:11], s[8:9], 12
	s_ashr_i32 s6, s3, 31
	s_add_u32 s3, s10, s3
	s_addc_u32 s9, s11, s6
	s_ashr_i32 s10, s7, 31
	s_add_u32 s6, s3, s7
	s_addc_u32 s7, s9, s10
	s_lshl_b64 s[6:7], s[6:7], 9
	s_add_u32 s3, s4, s6
	s_addc_u32 s5, s5, s7
	s_lshl_b32 s4, s2, 4
	s_and_b32 s9, s4, 0x70
	s_lshl_b32 s4, s9, 2
	s_add_u32 s4, s3, s4
	v_and_b32_e32 v1, 12, v1
	s_movk_i32 s3, 0x384
	s_addc_u32 s5, s5, 0
	v_mov_b32_e32 v33, 49
	s_movk_i32 s3, 0x50
	v_mov_b32_e32 v28, v0
	v_mul_u32_u24_e32 v29, 0x445, v28
	v_lshrrev_b32_e32 v32, 2, v28
	v_lshlrev_b32_e32 v34, 4, v28
	v_mul_lo_u16_sdwa v29, v29, v33 dst_sel:DWORD dst_unused:UNUSED_PAD src0_sel:WORD_1 src1_sel:DWORD
	v_and_b32_e32 v34, 48, v34
	v_add_lshl_u32 v30, v32, v29, 9
	v_add_u32_e32 v30, v30, v34
	global_load_dwordx4 v[8:11], v30, s[4:5]
	v_mad_u32_u24 v24, v32, s3, v34
	v_or_b32_e32 v28, 0x100, v0
	v_mul_u32_u24_e32 v29, 0x445, v28
	v_lshrrev_b32_e32 v32, 2, v28
	v_lshlrev_b32_e32 v34, 4, v28
	v_mul_lo_u16_sdwa v29, v29, v33 dst_sel:DWORD dst_unused:UNUSED_PAD src0_sel:WORD_1 src1_sel:DWORD
	v_and_b32_e32 v34, 48, v34
	v_add_lshl_u32 v31, v32, v29, 9
	v_add_u32_e32 v31, v31, v34
	global_load_dwordx4 v[12:15], v31, s[4:5]
	v_mad_u32_u24 v25, v32, s3, v34
	v_or_b32_e32 v28, 0x200, v0
	v_mul_u32_u24_e32 v29, 0x445, v28
	v_lshrrev_b32_e32 v32, 2, v28
	v_lshlrev_b32_e32 v34, 4, v28
	v_mul_lo_u16_sdwa v29, v29, v33 dst_sel:DWORD dst_unused:UNUSED_PAD src0_sel:WORD_1 src1_sel:DWORD
	v_and_b32_e32 v34, 48, v34
	v_add_lshl_u32 v36, v32, v29, 9
	v_add_u32_e32 v36, v36, v34
	global_load_dwordx4 v[16:19], v36, s[4:5]
	v_mad_u32_u24 v26, v32, s3, v34
	v_or_b32_e32 v28, 0x300, v0
	v_min_u32_e32 v28, 0x383, v28
	v_mul_u32_u24_e32 v29, 0x445, v28
	v_lshrrev_b32_e32 v32, 2, v28
	v_lshlrev_b32_e32 v34, 4, v28
	v_mul_lo_u16_sdwa v29, v29, v33 dst_sel:DWORD dst_unused:UNUSED_PAD src0_sel:WORD_1 src1_sel:DWORD
	v_and_b32_e32 v34, 48, v34
	v_add_lshl_u32 v37, v32, v29, 9
	v_add_u32_e32 v37, v37, v34
	global_load_dwordx4 v[20:23], v37, s[4:5]
	v_mad_u32_u24 v27, v32, s3, v34
	v_cmp_gt_u32_e32 vcc, 64, v0
	s_waitcnt vmcnt(4)
	s_and_saveexec_b64 s[6:7], vcc
	ds_write2st64_b32 v42, v40, v41 offset0:70 offset1:71
	s_or_b64 exec, exec, s[6:7]
	s_waitcnt vmcnt(3)
	ds_write_b128 v24, v[8:11]
	s_waitcnt vmcnt(2)
	ds_write_b128 v25, v[12:15]
	s_waitcnt vmcnt(1)
	ds_write_b128 v26, v[16:19]
	s_load_dwordx2 s[10:11], s[0:1], 0x40
	s_movk_i32 s0, 0x84
	v_cmp_gt_u32_e32 vcc, s0, v0
	s_waitcnt vmcnt(0)
	s_and_saveexec_b64 s[0:1], vcc
	ds_write_b128 v27, v[20:23]
